# baseline (speedup 1.0000x reference)
.Lat_spec_ok:
	v_and_b32_e32 v31, 7, v0
	v_bitop3_b32 v33, v10, v0, 7 bitop3:0x78
	v_lshlrev_b32_e32 v1, 7, v1
	v_mbcnt_lo_u32_b32 v34, -1, 0
	v_lshlrev_b32_e32 v89, 4, v33
	v_bitop3_b32 v31, v10, v31, 4 bitop3:0x36
	v_xor_b32_e32 v33, v13, v0
	v_mov_b32_e32 v13, v12
	v_lshlrev_b32_e32 v87, 4, v11
	s_movk_i32 s1, 0x70
	v_lshlrev_b32_e32 v98, 2, v10
	v_mov_b32_e32 v10, v12
	v_mov_b32_e32 v11, v12
	v_mbcnt_hi_u32_b32 v0, -1, v34
	v_lshl_or_b32 v91, v31, 4, v1
	v_lshlrev_b32_e32 v31, 4, v33
	v_mov_b64_e32 v[36:37], v[12:13]
	v_mov_b64_e32 v[40:41], v[12:13]
	v_mov_b64_e32 v[44:45], v[12:13]
	v_mov_b64_e32 v[48:49], v[12:13]
	v_mov_b64_e32 v[52:53], v[12:13]
	s_mov_b32 s17, 0
	v_mov_b64_e32 v[100:101], 0
	s_mov_b64 s[14:15], -1
	s_mov_b32 s5, 0xff800000
	s_mov_b32 s7, 0x41000000
	s_mov_b32 s12, 0x3c003c00
	v_mov_b32_e32 v30, 0x3c003c00
	v_mov_b32_e32 v54, v12
	v_mov_b64_e32 v[34:35], v[10:11]
	v_mov_b64_e32 v[38:39], v[10:11]
	v_mov_b64_e32 v[42:43], v[10:11]
	v_mov_b64_e32 v[46:47], v[10:11]
	v_mov_b64_e32 v[50:51], v[10:11]
	v_and_or_b32 v99, v31, s1, v32
	s_mov_b32 s9, 0
	s_waitcnt vmcnt(3)
	ds_write_b128 v99, v[22:25]
	ds_write_b128 v90, v[14:17] offset:8192
	s_waitcnt vmcnt(2)
	ds_write_b128 v99, v[18:21] offset:4096
	s_waitcnt vmcnt(1)
	ds_write_b128 v90, v[26:29] offset:12288
	s_waitcnt vmcnt(0)
	s_cmp_gt_i32 s11, 3
	s_cbranch_scc0 .LBB1_20

.LBB1_27:
	s_waitcnt lgkmcnt(0)
	s_barrier
	s_lshl_b32 s10, s9, 14
	s_lshl_b32 s13, 1, s0
	s_and_b32 s0, s13, s4
	v_or_b32_e32 v10, s10, v89
	s_cmp_eq_u32 s0, 0
	v_mov_b32_e32 v55, v54
	v_mov_b32_e32 v56, v54
	v_mov_b32_e32 v57, v54
	v_add_u32_e32 v106, v10, v1
	v_add_u32_e32 v105, s10, v91
	s_cbranch_scc1 .LBB1_32
	ds_read_b128 v[58:61], v106
	ds_read_b128 v[62:65], v105
	v_lshrrev_b64 v[10:11], v98, v[102:103]
	v_bfe_i32 v13, v10, 1, 1
	v_bfe_i32 v31, v10, 2, 1
	s_waitcnt lgkmcnt(1)
	v_mfma_f32_16x16x32_f16 v[58:61], v[58:61], v[2:5], v[54:57]
	v_bfe_i32 v32, v10, 3, 1
	v_bfe_i32 v11, v10, 0, 1
	s_waitcnt lgkmcnt(0)
	v_mfma_f32_16x16x32_f16 v[58:61], v[62:65], v[6:9], v[58:61]
	s_nop 7
	v_bitop3_b32 v10, v59, s5, v13 bitop3:0xe4
	v_bitop3_b32 v31, v60, s5, v31 bitop3:0xe4
	v_bitop3_b32 v13, v61, s5, v32 bitop3:0xe4
	v_max_f32_e32 v32, v13, v13
	v_max_f32_e32 v33, v31, v31
	v_bitop3_b32 v11, v58, s5, v11 bitop3:0xe4
	v_max_f32_e32 v32, v33, v32
	v_max3_f32 v32, v11, v10, v32
	v_cmp_lt_f32_e32 vcc, s7, v32
	s_or_b64 s[0:1], s[14:15], vcc
	v_cndmask_b32_e64 v33, 0, 1, s[0:1]
	v_cmp_ne_u32_e32 vcc, 0, v33
	s_cbranch_vccz .LBB1_35
	v_and_b32_e32 v58, 64, v0
	v_xor_b32_e32 v33, 16, v0
	v_add_u32_e32 v58, 64, v58
	v_cmp_lt_i32_e32 vcc, v33, v58
	s_mov_b64 s[22:23], 0
	s_nop 0
	v_cndmask_b32_e32 v33, v0, v33, vcc
	v_lshlrev_b32_e32 v33, 2, v33
	ds_bpermute_b32 v33, v33, v32
	v_max_f32_e32 v32, v32, v32
	s_waitcnt lgkmcnt(0)
	v_max_f32_e32 v33, v33, v33
	v_max_f32_e32 v32, v32, v33
	v_mov_b32_e32 v33, v32
	s_nop 1
	v_permlane32_swap_b32_e32 v32, v33
	v_max_f32_e32 v33, v33, v33
	v_max_f32_e32 v32, v32, v32
	v_max_f32_e32 v32, v32, v33
	v_cmp_nlg_f32_e32 vcc, s5, v32
	v_cmp_lg_f32_e64 s[0:1], s5, v32
	s_and_saveexec_b64 s[24:25], s[0:1]
	v_cmp_lt_f32_e64 s[0:1], s7, v32
	s_or_b64 s[0:1], s[14:15], s[0:1]
	s_and_b64 s[22:23], s[0:1], exec
	s_or_b64 exec, exec, s[24:25]
	v_exp_f32_e64 v33, -v32
	v_cndmask_b32_e64 v32, 0, v32, s[22:23]
	v_sub_f32_e32 v11, v11, v32
	v_sub_f32_e32 v10, v10, v32
	v_cndmask_b32_e64 v33, v33, 1.0, s[14:15]
	v_cndmask_b32_e64 v66, 1.0, v33, s[22:23]
	v_pk_mul_f32 v[60:61], v[48:49], v[66:67] op_sel_hi:[1,0]
	v_pk_mul_f32 v[58:59], v[46:47], v[66:67] op_sel_hi:[1,0]
	v_pk_mul_f32 v[64:65], v[66:67], v[44:45] op_sel_hi:[0,1]
	v_pk_mul_f32 v[62:63], v[66:67], v[42:43] op_sel_hi:[0,1]
	v_pk_mul_f32 v[80:81], v[66:67], v[40:41] op_sel_hi:[0,1]
	v_pk_mul_f32 v[78:79], v[66:67], v[38:39] op_sel_hi:[0,1]
	v_pk_mul_f32 v[84:85], v[66:67], v[36:37] op_sel_hi:[0,1]
	v_pk_mul_f32 v[82:83], v[66:67], v[34:35] op_sel_hi:[0,1]
	v_pk_mul_f32 v[68:69], v[52:53], v[66:67] op_sel_hi:[1,0]
	v_pk_mul_f32 v[66:67], v[50:51], v[66:67] op_sel_hi:[1,0]
	v_sub_f32_e32 v31, v31, v32
	v_sub_f32_e32 v13, v13, v32
	v_sub_f32_e32 v104, v54, v32
	s_and_b64 s[0:1], s[14:15], vcc
	s_branch .LBB1_36

.LBB1_34:
	s_xor_b32 s9, s9, 1
	s_lshl_b32 s10, s9, 14
	s_waitcnt vmcnt(0)
	v_or_b32_e32 v10, s10, v99
	v_mov_b64_e32 v[102:103], v[100:101]
	v_or_b32_e32 v11, s10, v90
	ds_write_b128 v10, v[22:25]
	ds_write_b128 v11, v[14:17] offset:8192
	ds_write_b128 v10, v[18:21] offset:4096
	ds_write_b128 v11, v[26:29] offset:12288
	s_cbranch_execnz .LBB1_46
	s_branch .LBB1_47

.LBB1_44:
	v_exp_f32_e32 v10, v68
	v_exp_f32_e32 v11, v69
	v_exp_f32_e32 v32, v64
	v_exp_f32_e32 v13, v70
	v_exp_f32_e32 v31, v71
	v_cvt_pkrtz_f16_f32 v64, v10, v11
	v_add_u32_e32 v10, s10, v87
	ds_read_b128 v[72:75], v10 offset:8192
	ds_read_b128 v[76:79], v10 offset:10240
	v_exp_f32_e32 v33, v65
	v_exp_f32_e32 v54, v66
	v_exp_f32_e32 v55, v67
	ds_read_b128 v[80:83], v10 offset:12288
	ds_read_b128 v[106:109], v10 offset:9216
	s_mov_b32 s14, s12
	s_mov_b32 s15, s12
	s_mov_b32 s13, s12
	v_mov_b64_e32 v[70:71], s[14:15]
	v_cvt_pkrtz_f16_f32 v65, v13, v31
	v_cvt_pkrtz_f16_f32 v67, v54, v55
	v_cvt_pkrtz_f16_f32 v66, v32, v33
	v_exp_f32_e32 v84, v60
	v_exp_f32_e32 v85, v61
	v_mov_b64_e32 v[68:69], s[12:13]
	v_exp_f32_e32 v11, v62
	s_waitcnt lgkmcnt(3)
	v_mfma_f32_16x16x32_f16 v[46:49], v[72:75], v[64:67], v[46:49]
	v_exp_f32_e32 v13, v63
	ds_read_b128 v[60:63], v10 offset:14336
	ds_read_b128 v[110:113], v10 offset:11264
	v_exp_f32_e32 v31, v56
	s_waitcnt lgkmcnt(4)
	v_mfma_f32_16x16x32_f16 v[42:45], v[76:79], v[64:67], v[42:45]
	v_exp_f32_e32 v72, v57
	ds_read_b128 v[54:57], v10 offset:13312
	v_exp_f32_e32 v73, v58
	s_waitcnt lgkmcnt(4)
	v_mfma_f32_16x16x32_f16 v[38:41], v[80:83], v[64:67], v[38:41]
	ds_read_b128 v[78:81], v10 offset:15360
	v_exp_f32_e32 v74, v59
	v_cvt_pkrtz_f16_f32 v58, v84, v85
	v_mfma_f32_16x16x32_f16 v[50:53], v[68:71], v[64:67], v[50:53]
	v_cvt_pkrtz_f16_f32 v59, v11, v13
	s_waitcnt lgkmcnt(3)
	v_mfma_f32_16x16x32_f16 v[34:37], v[60:63], v[64:67], v[34:37]
	v_cvt_pkrtz_f16_f32 v61, v73, v74
	v_cvt_pkrtz_f16_f32 v60, v31, v72
	s_nop 1
	v_mfma_f32_16x16x32_f16 v[50:53], v[68:71], v[58:61], v[50:53]
	v_mfma_f32_16x16x32_f16 v[46:49], v[106:109], v[58:61], v[46:49]
	s_waitcnt lgkmcnt(2)
	v_mfma_f32_16x16x32_f16 v[42:45], v[110:113], v[58:61], v[42:45]
	s_waitcnt lgkmcnt(1)
	v_mfma_f32_16x16x32_f16 v[38:41], v[54:57], v[58:61], v[38:41]
	s_waitcnt lgkmcnt(0)
	v_mfma_f32_16x16x32_f16 v[34:37], v[78:81], v[58:61], v[34:37]
	s_andn2_b64 vcc, exec, s[18:19]
	s_cbranch_vccnz .Lat_exit4
	s_xor_b32 s9, s9, 1
	s_lshl_b32 s10, s9, 14
	s_waitcnt vmcnt(0)
	v_or_b32_e32 v10, s10, v99
	v_mov_b64_e32 v[102:103], v[100:101]
	v_or_b32_e32 v11, s10, v90
	ds_write_b128 v10, v[22:25]
	ds_write_b128 v11, v[14:17] offset:8192
	ds_write_b128 v10, v[18:21] offset:4096
	ds_write_b128 v11, v[26:29] offset:12288
	s_mov_b64 s[14:15], s[0:1]
	s_mov_b32 s0, s16
	v_mov_b32_e32 v54, v104
	s_cmp_gt_i32 s11, 3
	s_cbranch_scc1 .LBB1_17
	s_branch .LBB1_20
